# hyena layer-1 hosting + batched staging loads + down-GEMM epilogue gate scales preloaded (was 8 serialized load/wait steps) + hyena-out YC loads batched
# speedup vs baseline: 1.0179x; 1.0050x over previous
; #define GAS __attribute__((address_space(1)))
; __device__ __forceinline__ void hy_out_item(Frame& F, int l, int item, LAS unsigned char* lb) {
;     ...
;     {   const GAS bf16* yc = (const GAS bf16*)(F.ws + WS_YC);
; #pragma unroll
;         for (int k = 0; k < 8; ++k) { const int i = tid + NTHR * k, cc = i >> 4, q = i & 15; const v2u w_ = *(const GAS v2u*)(yc + ((size_t)cc * BATCH + b) * SEQ + t0 + 4 * q);
;             const f32x4 v = (f32x4){__uint_as_float(w_.x << 16), __uint_as_float(w_.x & 0xffff0000u), __uint_as_float(w_.y << 16), __uint_as_float(w_.y & 0xffff0000u)};
;             ys[(4 * q) * 260 + cc] = v[0]; ys[(4 * q + 1) * 260 + cc] = v[1]; ys[(4 * q + 2) * 260 + cc] = v[2]; ys[(4 * q + 3) * 260 + cc] = v[3]; } }
;     const GAS bf16* p = (const GAS bf16*)(F.ws + WS_PROJ) + ((size_t)b * SEQ + tq0) * NPROJ + PC_HX0 + 8 * cg;
.LBB0_900:
	s_ashr_i32 s2, s25, 6
	s_ashr_i32 s3, s2, 31
	s_waitcnt vmcnt(0)
	v_mov_b32_e32 v6, v1
	s_and_b32 s4, s24, 0xfc0
	s_lshl_b64 s[6:7], s[2:3], 13
	s_add_u32 s5, s21, s6
	v_lshlrev_b32_e32 v2, 2, v6
	s_addc_u32 s7, s22, s7
	s_lshl_b32 s6, s4, 1
	v_and_b32_e32 v4, 60, v2
	s_add_u32 s6, s5, s6
	v_lshlrev_b32_e32 v182, 1, v4
	v_mad_u32_u24 v7, v4, s30, 0
	v_ashrrev_i32_e32 v4, 4, v6
	s_addc_u32 s7, s7, 0
	v_ashrrev_i32_e32 v5, 31, v4
	v_lshl_add_u64 v[2:3], s[6:7], 0, v[182:183]
	v_lshlrev_b64 v[8:9], 15, v[4:5]
	v_lshl_add_u64 v[8:9], v[2:3], 0, v[8:9]
	global_load_dwordx2 v[214:215], v[8:9], off
	v_ashrrev_i32_e32 v196, 3, v6
	v_and_b32_e32 v180, -4, v196
	s_lshl_b64 s[2:3], s[2:3], 12
	v_mov_b32_e32 v141, v183
	v_add_u32_e32 v4, 0x200, v6
	v_ashrrev_i32_e32 v4, 4, v4
	v_ashrrev_i32_e32 v5, 31, v4
	v_lshlrev_b64 v[8:9], 15, v[4:5]
	v_lshl_add_u64 v[8:9], v[2:3], 0, v[8:9]
	global_load_dwordx2 v[216:217], v[8:9], off
	v_add_u32_e32 v4, 0x400, v6
	v_ashrrev_i32_e32 v4, 4, v4
	v_ashrrev_i32_e32 v5, 31, v4
	v_lshlrev_b64 v[8:9], 15, v[4:5]
	v_lshl_add_u64 v[8:9], v[2:3], 0, v[8:9]
	global_load_dwordx2 v[218:219], v[8:9], off
	v_add_u32_e32 v4, 0x600, v6
	v_ashrrev_i32_e32 v4, 4, v4
	v_ashrrev_i32_e32 v5, 31, v4
	v_lshlrev_b64 v[8:9], 15, v[4:5]
	v_lshl_add_u64 v[8:9], v[2:3], 0, v[8:9]
	global_load_dwordx2 v[220:221], v[8:9], off
	v_add_u32_e32 v4, 0x800, v6
	v_ashrrev_i32_e32 v4, 4, v4
	v_ashrrev_i32_e32 v5, 31, v4
	v_lshlrev_b64 v[8:9], 15, v[4:5]
	v_lshl_add_u64 v[8:9], v[2:3], 0, v[8:9]
	global_load_dwordx2 v[222:223], v[8:9], off
	v_add_u32_e32 v4, 0xa00, v6
	v_ashrrev_i32_e32 v4, 4, v4
	v_ashrrev_i32_e32 v5, 31, v4
	v_lshlrev_b64 v[8:9], 15, v[4:5]
	v_lshl_add_u64 v[8:9], v[2:3], 0, v[8:9]
	global_load_dwordx2 v[234:235], v[8:9], off
	v_add_u32_e32 v4, 0xc00, v6
	v_ashrrev_i32_e32 v4, 4, v4
	v_ashrrev_i32_e32 v5, 31, v4
	v_lshlrev_b64 v[8:9], 15, v[4:5]
	v_lshl_add_u64 v[8:9], v[2:3], 0, v[8:9]
	global_load_dwordx2 v[246:247], v[8:9], off
	v_add_u32_e32 v4, 0xe00, v6
	v_ashrrev_i32_e32 v4, 4, v4
	v_ashrrev_i32_e32 v5, 31, v4
	v_lshlrev_b64 v[8:9], 15, v[4:5]
	v_lshl_add_u64 v[2:3], v[2:3], 0, v[8:9]
	global_load_dwordx2 v[248:249], v[2:3], off
	s_waitcnt vmcnt(0)
	v_ashrrev_i32_e32 v4, 4, v6
	v_lshl_add_u32 v4, v4, 2, v7
	v_lshlrev_b32_e32 v5, 16, v214
	v_and_b32_e32 v214, 0xffff0000, v214
	v_lshlrev_b32_e32 v10, 16, v215
	v_and_b32_e32 v215, 0xffff0000, v215
	ds_write_b32 v4, v5
	ds_write_b32 v4, v214 offset:1040
	ds_write_b32 v4, v10 offset:2080
	ds_write_b32 v4, v215 offset:3120
	v_add_u32_e32 v4, 0x200, v6
	v_ashrrev_i32_e32 v4, 4, v4
	v_lshl_add_u32 v4, v4, 2, v7
	v_lshlrev_b32_e32 v5, 16, v216
	v_and_b32_e32 v216, 0xffff0000, v216
	v_lshlrev_b32_e32 v10, 16, v217
	v_and_b32_e32 v217, 0xffff0000, v217
	ds_write_b32 v4, v5
	ds_write_b32 v4, v216 offset:1040
	ds_write_b32 v4, v10 offset:2080
	ds_write_b32 v4, v217 offset:3120
	v_add_u32_e32 v4, 0x400, v6
	v_ashrrev_i32_e32 v4, 4, v4
	v_lshl_add_u32 v4, v4, 2, v7
	v_lshlrev_b32_e32 v5, 16, v218
	v_and_b32_e32 v218, 0xffff0000, v218
	v_lshlrev_b32_e32 v10, 16, v219
	v_and_b32_e32 v219, 0xffff0000, v219
	ds_write_b32 v4, v5
	ds_write_b32 v4, v218 offset:1040
	ds_write_b32 v4, v10 offset:2080
	ds_write_b32 v4, v219 offset:3120
	v_add_u32_e32 v4, 0x600, v6
	v_ashrrev_i32_e32 v4, 4, v4
	v_lshl_add_u32 v4, v4, 2, v7
	v_lshlrev_b32_e32 v5, 16, v220
	v_and_b32_e32 v220, 0xffff0000, v220
	v_lshlrev_b32_e32 v10, 16, v221
	v_and_b32_e32 v221, 0xffff0000, v221
	ds_write_b32 v4, v5
	ds_write_b32 v4, v220 offset:1040
	ds_write_b32 v4, v10 offset:2080
	ds_write_b32 v4, v221 offset:3120
	v_add_u32_e32 v4, 0x800, v6
	v_ashrrev_i32_e32 v4, 4, v4
	v_lshl_add_u32 v4, v4, 2, v7
	v_lshlrev_b32_e32 v5, 16, v222
	v_and_b32_e32 v222, 0xffff0000, v222
	v_lshlrev_b32_e32 v10, 16, v223
	v_and_b32_e32 v223, 0xffff0000, v223
	ds_write_b32 v4, v5
	ds_write_b32 v4, v222 offset:1040
	ds_write_b32 v4, v10 offset:2080
	ds_write_b32 v4, v223 offset:3120
	v_add_u32_e32 v4, 0xa00, v6
	v_ashrrev_i32_e32 v4, 4, v4
	v_lshl_add_u32 v4, v4, 2, v7
	v_lshlrev_b32_e32 v5, 16, v234
	v_and_b32_e32 v234, 0xffff0000, v234
	v_lshlrev_b32_e32 v10, 16, v235
	v_and_b32_e32 v235, 0xffff0000, v235
	ds_write_b32 v4, v5
	ds_write_b32 v4, v234 offset:1040
	ds_write_b32 v4, v10 offset:2080
	ds_write_b32 v4, v235 offset:3120
	v_add_u32_e32 v4, 0xc00, v6
	v_ashrrev_i32_e32 v4, 4, v4
	v_lshl_add_u32 v4, v4, 2, v7
	v_lshlrev_b32_e32 v5, 16, v246
	v_and_b32_e32 v246, 0xffff0000, v246
	v_lshlrev_b32_e32 v10, 16, v247
	v_and_b32_e32 v247, 0xffff0000, v247
	ds_write_b32 v4, v5
	ds_write_b32 v4, v246 offset:1040
	ds_write_b32 v4, v10 offset:2080
	ds_write_b32 v4, v247 offset:3120
	v_add_u32_e32 v4, 0xe00, v6
	v_ashrrev_i32_e32 v4, 4, v4
	v_lshl_add_u32 v4, v4, 2, v7
	v_lshlrev_b32_e32 v5, 16, v248
	v_and_b32_e32 v248, 0xffff0000, v248
	v_lshlrev_b32_e32 v10, 16, v249
	v_and_b32_e32 v249, 0xffff0000, v249
	ds_write_b32 v4, v5
	ds_write_b32 v4, v248 offset:1040
	ds_write_b32 v4, v10 offset:2080
	ds_write_b32 v4, v249 offset:3120
	v_add_u32_e32 v4, s4, v180
	v_ashrrev_i32_e32 v5, 31, v4
	v_lshl_add_u64 v[138:139], s[2:3], 0, v[4:5]
	v_mov_b64_e32 v[2:3], s[58:59]
	v_lshlrev_b32_e32 v5, 3, v6
	v_mad_u64_u32 v[2:3], s[2:3], v138, s62, v[2:3]
	v_and_b32_e32 v10, 0xf8, v5
	v_mad_i32_i24 v3, v139, s62, v3
	v_lshlrev_b32_e32 v140, 1, v10
	v_lshl_add_u64 v[2:3], v[2:3], 0, v[140:141]
	s_mov_b64 s[2:3], 0x4400e00
	v_lshl_add_u64 v[142:143], v[2:3], 0, s[2:3]
	v_mov_b32_e32 v2, s72
	ds_read_b128 v[6:9], v2
	s_waitcnt lgkmcnt(0)
	v_readfirstlane_b32 s26, v6
	v_readfirstlane_b32 s27, v7
	v_readfirstlane_b32 s16, v8
	v_readfirstlane_b32 s17, v9
	v_add_u32_e32 v2, -1, v4
	v_cmp_gt_u32_e64 s[6:7], s71, v2
	v_mov_b32_e32 v102, 0
	v_mov_b32_e32 v98, 0
	v_mov_b32_e32 v99, 0
	v_mov_b32_e32 v100, 0
	v_mov_b32_e32 v101, 0
	s_and_saveexec_b64 s[2:3], s[6:7]
	s_cbranch_execz .LBB0_902
	v_add_co_u32_e32 v2, vcc, 0xfffff000, v142
	s_nop 1
	v_addc_co_u32_e32 v3, vcc, -1, v143, vcc
	global_load_dwordx4 v[98:101], v[2:3], off offset:-512

; __device__ __forceinline__ unsigned cvt_pk_bf16(float lo, float hi) { unsigned r; asm volatile("v_cvt_pk_bf16_f32 %0, %1, %2" : "=v"(r) : "v"(lo), "v"(hi)); return r; }
;     __device__ __forceinline__ void operator()(const f32x4 (&acc)[2][2][4][2], const Unit& u, int wr, int wc, int fr, int fq) const {
;     ...
;             for (int m = 0; m < 4; ++m) { const int row = row0 + ai * HALF + m * 16; const float s = (rowscale ? rowscale[row] : 1.f) * mul; bf16_t* rowp = O + (size_t)row * ldc + col0;
; #pragma unroll
;                 for (int bj = 0; bj < 2; ++bj) { const f32x4 v0 = acc[ai][bj][m][0] * s, v1 = acc[ai][bj][m][1] * s;
;                     u32x4 w; w.x = cvt_pk_bf16(v0[0], v0[1]); w.y = cvt_pk_bf16(v0[2], v0[3]); w.z = cvt_pk_bf16(v1[0], v1[1]); w.w = cvt_pk_bf16(v1[2], v1[3]);
;                     *(u32x4*)(rowp + bj * HALF) = w; } }
.LBB0_1806:
	s_nop 15
	s_nop 15
	v_lshl_add_u32 v2, s51, 8, v172
	v_cndmask_b32_e64 v4, 0, 1, s[18:19]
	v_ashrrev_i32_e32 v3, 31, v2
	v_mov_b32_e32 v6, 0x3c800000
	v_cmp_ne_u32_e64 s[6:7], 1, v4
	s_andn2_b64 vcc, exec, s[18:19]
	v_mov_b32_e32 v8, 0x3c800000
	v_readlane_b32 s54, v255, 5
	s_cbranch_vccnz .LBB0_1808
	v_lshl_add_u64 v[4:5], v[2:3], 2, s[14:15]
	global_load_dword v246, v[4:5], off
	global_load_dword v247, v[4:5], off offset:64
	global_load_dword v248, v[4:5], off offset:128
	global_load_dword v249, v[4:5], off offset:192
	global_load_dword v250, v[4:5], off offset:512
	global_load_dword v251, v[4:5], off offset:576
	global_load_dword v252, v[4:5], off offset:640
	global_load_dword v253, v[4:5], off offset:704
	s_waitcnt vmcnt(0)
	v_mul_f32_e32 v8, 0x3c800000, v246
.LBB0_1808:
	v_lshl_or_b32 v4, s50, 8, v174
	v_lshlrev_b64 v[10:11], 11, v[2:3]
	v_ashrrev_i32_e32 v5, 31, v4
	v_lshl_add_u64 v[10:11], s[12:13], 0, v[10:11]
	v_lshl_add_u64 v[14:15], v[4:5], 1, v[10:11]
	v_pk_mul_f32 v[12:13], v[160:161], v[8:9] op_sel_hi:[1,0]
	v_pk_mul_f32 v[10:11], v[158:159], v[8:9] op_sel_hi:[1,0]
	v_pk_mul_f32 v[16:17], v[156:157], v[8:9] op_sel_hi:[1,0]
	v_pk_mul_f32 v[18:19], v[154:155], v[8:9] op_sel_hi:[1,0]
	v_cvt_pk_bf16_f32 v10, v10, v11
	v_cvt_pk_bf16_f32 v11, v12, v13
	s_and_b64 vcc, exec, s[6:7]
	v_cvt_pk_bf16_f32 v12, v18, v19
	v_cvt_pk_bf16_f32 v13, v16, v17
	global_store_dwordx4 v[14:15], v[10:13], off
	v_pk_mul_f32 v[16:17], v[148:149], v[8:9] op_sel_hi:[1,0]
	v_pk_mul_f32 v[18:19], v[146:147], v[8:9] op_sel_hi:[1,0]
	v_pk_mul_f32 v[10:11], v[152:153], v[8:9] op_sel_hi:[1,0]
	v_pk_mul_f32 v[12:13], v[150:151], v[8:9] op_sel_hi:[1,0]
	s_nop 0
	v_cvt_pk_bf16_f32 v8, v12, v13
	v_cvt_pk_bf16_f32 v9, v10, v11
	v_cvt_pk_bf16_f32 v10, v18, v19
	v_cvt_pk_bf16_f32 v11, v16, v17
	global_store_dwordx4 v[14:15], v[8:11], off offset:256
	s_nop 1
	v_or_b32_e32 v8, 16, v2
	v_ashrrev_i32_e32 v9, 31, v8
	s_cbranch_vccnz .LBB0_1810
	v_lshl_add_u64 v[6:7], v[8:9], 2, s[14:15]
	v_mul_f32_e32 v6, 0x3c800000, v247
.LBB0_1810:
	v_lshlrev_b64 v[8:9], 11, v[8:9]
	v_lshl_add_u64 v[8:9], s[12:13], 0, v[8:9]
	v_lshl_add_u64 v[12:13], v[4:5], 1, v[8:9]
	v_pk_mul_f32 v[10:11], v[144:145], v[6:7] op_sel_hi:[1,0]
	v_pk_mul_f32 v[8:9], v[142:143], v[6:7] op_sel_hi:[1,0]
	v_pk_mul_f32 v[14:15], v[140:141], v[6:7] op_sel_hi:[1,0]
	v_pk_mul_f32 v[16:17], v[138:139], v[6:7] op_sel_hi:[1,0]
	v_cvt_pk_bf16_f32 v8, v8, v9
	v_cvt_pk_bf16_f32 v9, v10, v11
	s_and_b64 vcc, exec, s[6:7]
	v_cvt_pk_bf16_f32 v10, v16, v17
	v_cvt_pk_bf16_f32 v11, v14, v15
	global_store_dwordx4 v[12:13], v[8:11], off
	v_pk_mul_f32 v[14:15], v[132:133], v[6:7] op_sel_hi:[1,0]
	v_pk_mul_f32 v[16:17], v[130:131], v[6:7] op_sel_hi:[1,0]
	v_pk_mul_f32 v[8:9], v[136:137], v[6:7] op_sel_hi:[1,0]
	v_pk_mul_f32 v[10:11], v[134:135], v[6:7] op_sel_hi:[1,0]
	s_mov_b64 s[56:57], s[60:61]
	v_cvt_pk_bf16_f32 v6, v10, v11
	v_cvt_pk_bf16_f32 v7, v8, v9
	v_cvt_pk_bf16_f32 v8, v16, v17
	v_or_b32_e32 v10, 32, v2
	v_cvt_pk_bf16_f32 v9, v14, v15
	global_store_dwordx4 v[12:13], v[6:9], off offset:256
	v_ashrrev_i32_e32 v11, 31, v10
	s_nop 0
	v_mov_b32_e32 v6, 0x3c800000
	v_mov_b32_e32 v8, 0x3c800000
	s_cbranch_vccnz .LBB0_1812
	v_lshl_add_u64 v[8:9], v[10:11], 2, s[14:15]
	v_mul_f32_e32 v8, 0x3c800000, v248
.LBB0_1812:
	v_lshlrev_b64 v[10:11], 11, v[10:11]
	v_lshl_add_u64 v[10:11], s[12:13], 0, v[10:11]
	v_lshl_add_u64 v[14:15], v[4:5], 1, v[10:11]
	v_pk_mul_f32 v[12:13], v[128:129], v[8:9] op_sel_hi:[1,0]
	v_pk_mul_f32 v[10:11], v[126:127], v[8:9] op_sel_hi:[1,0]
	v_pk_mul_f32 v[16:17], v[124:125], v[8:9] op_sel_hi:[1,0]
	v_pk_mul_f32 v[18:19], v[122:123], v[8:9] op_sel_hi:[1,0]
	v_cvt_pk_bf16_f32 v10, v10, v11
	v_cvt_pk_bf16_f32 v11, v12, v13
	s_and_b64 vcc, exec, s[6:7]
	v_cvt_pk_bf16_f32 v12, v18, v19
	v_cvt_pk_bf16_f32 v13, v16, v17
	global_store_dwordx4 v[14:15], v[10:13], off
	v_pk_mul_f32 v[16:17], v[116:117], v[8:9] op_sel_hi:[1,0]
	v_pk_mul_f32 v[18:19], v[114:115], v[8:9] op_sel_hi:[1,0]
	v_pk_mul_f32 v[10:11], v[120:121], v[8:9] op_sel_hi:[1,0]
	v_pk_mul_f32 v[12:13], v[118:119], v[8:9] op_sel_hi:[1,0]
	s_nop 0
	v_cvt_pk_bf16_f32 v8, v12, v13
	v_cvt_pk_bf16_f32 v9, v10, v11
	v_cvt_pk_bf16_f32 v10, v18, v19
	v_cvt_pk_bf16_f32 v11, v16, v17
	global_store_dwordx4 v[14:15], v[8:11], off offset:256
	s_nop 1
	v_or_b32_e32 v8, 48, v2
	v_ashrrev_i32_e32 v9, 31, v8
	s_cbranch_vccnz .LBB0_1814
	v_lshl_add_u64 v[6:7], v[8:9], 2, s[14:15]
	v_mul_f32_e32 v6, 0x3c800000, v249
; __device__ __forceinline__ unsigned cvt_pk_bf16(float lo, float hi) { unsigned r; asm volatile("v_cvt_pk_bf16_f32 %0, %1, %2" : "=v"(r) : "v"(lo), "v"(hi)); return r; }
;     __device__ __forceinline__ void operator()(const f32x4 (&acc)[2][2][4][2], const Unit& u, int wr, int wc, int fr, int fq) const {
;     ...
;             for (int m = 0; m < 4; ++m) { const int row = row0 + ai * HALF + m * 16; const float s = (rowscale ? rowscale[row] : 1.f) * mul; bf16_t* rowp = O + (size_t)row * ldc + col0;
; #pragma unroll
;                 for (int bj = 0; bj < 2; ++bj) { const f32x4 v0 = acc[ai][bj][m][0] * s, v1 = acc[ai][bj][m][1] * s;
;                     u32x4 w; w.x = cvt_pk_bf16(v0[0], v0[1]); w.y = cvt_pk_bf16(v0[2], v0[3]); w.z = cvt_pk_bf16(v1[0], v1[1]); w.w = cvt_pk_bf16(v1[2], v1[3]);
;                     *(u32x4*)(rowp + bj * HALF) = w; } }
.LBB0_1814:
	v_lshlrev_b64 v[8:9], 11, v[8:9]
	v_lshl_add_u64 v[8:9], s[12:13], 0, v[8:9]
	v_lshl_add_u64 v[12:13], v[4:5], 1, v[8:9]
	v_pk_mul_f32 v[10:11], v[112:113], v[6:7] op_sel_hi:[1,0]
	v_pk_mul_f32 v[8:9], v[110:111], v[6:7] op_sel_hi:[1,0]
	v_pk_mul_f32 v[14:15], v[108:109], v[6:7] op_sel_hi:[1,0]
	v_pk_mul_f32 v[16:17], v[106:107], v[6:7] op_sel_hi:[1,0]
	v_cvt_pk_bf16_f32 v8, v8, v9
	v_cvt_pk_bf16_f32 v9, v10, v11
	s_and_b64 vcc, exec, s[6:7]
	v_cvt_pk_bf16_f32 v10, v16, v17
	v_cvt_pk_bf16_f32 v11, v14, v15
	global_store_dwordx4 v[12:13], v[8:11], off
	v_pk_mul_f32 v[14:15], v[100:101], v[6:7] op_sel_hi:[1,0]
	v_pk_mul_f32 v[16:17], v[98:99], v[6:7] op_sel_hi:[1,0]
	v_pk_mul_f32 v[8:9], v[104:105], v[6:7] op_sel_hi:[1,0]
	v_pk_mul_f32 v[10:11], v[102:103], v[6:7] op_sel_hi:[1,0]
	s_nop 0
	v_cvt_pk_bf16_f32 v6, v10, v11
	v_cvt_pk_bf16_f32 v7, v8, v9
	v_cvt_pk_bf16_f32 v8, v16, v17
	v_add_u32_e32 v10, 0x80, v2
	v_cvt_pk_bf16_f32 v9, v14, v15
	global_store_dwordx4 v[12:13], v[6:9], off offset:256
	v_ashrrev_i32_e32 v11, 31, v10
	s_nop 0
	v_mov_b32_e32 v6, 0x3c800000
	v_mov_b32_e32 v8, 0x3c800000
	s_cbranch_vccnz .LBB0_1816
	v_lshl_add_u64 v[8:9], v[10:11], 2, s[14:15]
	v_mul_f32_e32 v8, 0x3c800000, v250
.LBB0_1816:
	v_lshlrev_b64 v[10:11], 11, v[10:11]
	v_lshl_add_u64 v[10:11], s[12:13], 0, v[10:11]
	v_lshl_add_u64 v[14:15], v[4:5], 1, v[10:11]
	v_pk_mul_f32 v[12:13], v[96:97], v[8:9] op_sel_hi:[1,0]
	v_pk_mul_f32 v[10:11], v[94:95], v[8:9] op_sel_hi:[1,0]
	v_pk_mul_f32 v[16:17], v[92:93], v[8:9] op_sel_hi:[1,0]
	v_pk_mul_f32 v[18:19], v[90:91], v[8:9] op_sel_hi:[1,0]
	v_cvt_pk_bf16_f32 v10, v10, v11
	v_cvt_pk_bf16_f32 v11, v12, v13
	s_and_b64 vcc, exec, s[6:7]
	v_cvt_pk_bf16_f32 v12, v18, v19
	v_cvt_pk_bf16_f32 v13, v16, v17
	global_store_dwordx4 v[14:15], v[10:13], off
	v_pk_mul_f32 v[16:17], v[84:85], v[8:9] op_sel_hi:[1,0]
	v_pk_mul_f32 v[18:19], v[82:83], v[8:9] op_sel_hi:[1,0]
	v_pk_mul_f32 v[10:11], v[88:89], v[8:9] op_sel_hi:[1,0]
	v_pk_mul_f32 v[12:13], v[86:87], v[8:9] op_sel_hi:[1,0]
	s_nop 0
	v_cvt_pk_bf16_f32 v8, v12, v13
	v_cvt_pk_bf16_f32 v9, v10, v11
	v_cvt_pk_bf16_f32 v10, v18, v19
	v_cvt_pk_bf16_f32 v11, v16, v17
	global_store_dwordx4 v[14:15], v[8:11], off offset:256
	s_nop 1
	v_add_u32_e32 v8, 0x90, v2
	v_ashrrev_i32_e32 v9, 31, v8
	s_cbranch_vccnz .LBB0_1818
	v_lshl_add_u64 v[6:7], v[8:9], 2, s[14:15]
	v_mul_f32_e32 v6, 0x3c800000, v251
.LBB0_1818:
	v_lshlrev_b64 v[8:9], 11, v[8:9]
	v_lshl_add_u64 v[8:9], s[12:13], 0, v[8:9]
	v_lshl_add_u64 v[12:13], v[4:5], 1, v[8:9]
	v_pk_mul_f32 v[10:11], v[80:81], v[6:7] op_sel_hi:[1,0]
	v_pk_mul_f32 v[8:9], v[78:79], v[6:7] op_sel_hi:[1,0]
	v_pk_mul_f32 v[14:15], v[76:77], v[6:7] op_sel_hi:[1,0]
	v_pk_mul_f32 v[16:17], v[74:75], v[6:7] op_sel_hi:[1,0]
	v_cvt_pk_bf16_f32 v8, v8, v9
	v_cvt_pk_bf16_f32 v9, v10, v11
	s_and_b64 vcc, exec, s[6:7]
	v_cvt_pk_bf16_f32 v10, v16, v17
	v_cvt_pk_bf16_f32 v11, v14, v15
	global_store_dwordx4 v[12:13], v[8:11], off
	v_pk_mul_f32 v[14:15], v[68:69], v[6:7] op_sel_hi:[1,0]
	v_pk_mul_f32 v[16:17], v[66:67], v[6:7] op_sel_hi:[1,0]
	v_pk_mul_f32 v[8:9], v[72:73], v[6:7] op_sel_hi:[1,0]
	v_pk_mul_f32 v[10:11], v[70:71], v[6:7] op_sel_hi:[1,0]
	s_nop 0
	v_cvt_pk_bf16_f32 v6, v10, v11
	v_cvt_pk_bf16_f32 v7, v8, v9
	v_cvt_pk_bf16_f32 v8, v16, v17
	v_add_u32_e32 v10, 0xa0, v2
	v_cvt_pk_bf16_f32 v9, v14, v15
	global_store_dwordx4 v[12:13], v[6:9], off offset:256
	v_ashrrev_i32_e32 v11, 31, v10
	s_nop 0
	v_mov_b32_e32 v6, 0x3c800000
	v_mov_b32_e32 v8, 0x3c800000
	s_cbranch_vccnz .LBB0_1820
	v_lshl_add_u64 v[8:9], v[10:11], 2, s[14:15]
	v_mul_f32_e32 v8, 0x3c800000, v252
.LBB0_1820:
	v_lshlrev_b64 v[10:11], 11, v[10:11]
	v_lshl_add_u64 v[10:11], s[12:13], 0, v[10:11]
	v_lshl_add_u64 v[14:15], v[4:5], 1, v[10:11]
	v_pk_mul_f32 v[10:11], v[62:63], v[8:9] op_sel_hi:[1,0]
	v_pk_mul_f32 v[12:13], v[64:65], v[8:9] op_sel_hi:[1,0]
	v_cvt_pk_bf16_f32 v10, v10, v11
	v_add_u32_e32 v2, 0xb0, v2
	v_cvt_pk_bf16_f32 v11, v12, v13
	v_pk_mul_f32 v[16:17], v[60:61], v[8:9] op_sel_hi:[1,0]
	v_pk_mul_f32 v[18:19], v[58:59], v[8:9] op_sel_hi:[1,0]
	s_and_b64 vcc, exec, s[6:7]
	v_cvt_pk_bf16_f32 v12, v18, v19
	v_cvt_pk_bf16_f32 v13, v16, v17
	global_store_dwordx4 v[14:15], v[10:13], off
	v_ashrrev_i32_e32 v3, 31, v2
	v_pk_mul_f32 v[16:17], v[52:53], v[8:9] op_sel_hi:[1,0]
	v_pk_mul_f32 v[10:11], v[56:57], v[8:9] op_sel_hi:[1,0]
	v_pk_mul_f32 v[12:13], v[54:55], v[8:9] op_sel_hi:[1,0]
	v_pk_mul_f32 v[18:19], v[50:51], v[8:9] op_sel_hi:[1,0]
	v_cvt_pk_bf16_f32 v8, v12, v13
	v_cvt_pk_bf16_f32 v9, v10, v11
	s_nop 0
	v_cvt_pk_bf16_f32 v10, v18, v19
	v_cvt_pk_bf16_f32 v11, v16, v17
	global_store_dwordx4 v[14:15], v[8:11], off offset:256
	s_cbranch_vccnz .LBB0_1822
	v_lshl_add_u64 v[6:7], v[2:3], 2, s[14:15]
	v_mul_f32_e32 v6, 0x3c800000, v253
